# baseline (speedup 1.0000x reference)
_Z2kBPKfPKDv4_jPKDF16_S0_S0_S0_Pf:
	v_lshrrev_b32_e32 v11, 7, v0
	s_load_dwordx8 s[4:11], s[0:1], 0x0
	v_lshl_or_b32 v2, s2, 2, v11
	s_mov_b32 s2, 0x4ec4ec4f
	v_mul_hi_i32 v1, v2, s2
	v_lshrrev_b32_e32 v3, 31, v1
	v_ashrrev_i32_e32 v1, 2, v1
	v_add_u32_e32 v1, v1, v3
	v_and_b32_e32 v108, 15, v0
	v_mad_u64_u32 v[4:5], s[2:3], v1, -13, v[2:3]
	v_lshlrev_b32_e32 v102, 4, v0
	v_mov_b32_e32 v103, 0
	v_lshl_or_b32 v10, v4, 4, v108
	s_waitcnt lgkmcnt(0)
	v_lshl_add_u64 v[4:5], s[8:9], 0, v[102:103]
	s_movk_i32 s2, 0x2000
	v_add_co_u32_e32 v6, vcc, s2, v4
	s_movk_i32 s2, 0x4000
	s_nop 0
	v_addc_co_u32_e32 v7, vcc, 0, v5, vcc
	v_add_co_u32_e32 v8, vcc, s2, v4
	s_movk_i32 s2, 0x6000
	s_nop 0
	v_addc_co_u32_e32 v9, vcc, 0, v5, vcc
	global_load_dwordx4 v[14:17], v102, s[8:9]
	global_load_dwordx4 v[18:21], v[6:7], off
	global_load_dwordx4 v[22:25], v[8:9], off
	v_add_co_u32_e32 v6, vcc, s2, v4
	s_mov_b32 s2, 0x8000
	s_nop 0
	v_addc_co_u32_e32 v7, vcc, 0, v5, vcc
	v_add_co_u32_e32 v8, vcc, s2, v4
	s_mov_b32 s2, 0xa000
	s_nop 0
	v_addc_co_u32_e32 v9, vcc, 0, v5, vcc
	global_load_dwordx4 v[26:29], v[6:7], off
	global_load_dwordx4 v[30:33], v[8:9], off
	v_add_co_u32_e32 v6, vcc, s2, v4
	s_mov_b32 s2, 0xc000
	s_nop 0
	v_addc_co_u32_e32 v7, vcc, 0, v5, vcc
	v_add_co_u32_e32 v8, vcc, s2, v4
	s_mov_b32 s2, 0xe000
	s_nop 0
	v_addc_co_u32_e32 v9, vcc, 0, v5, vcc
	v_add_co_u32_e32 v4, vcc, s2, v4
	s_movk_i32 s2, 0xc8
	s_nop 0
	v_addc_co_u32_e32 v5, vcc, 0, v5, vcc
	global_load_dwordx4 v[34:37], v[6:7], off
	global_load_dwordx4 v[38:41], v[8:9], off
	v_mov_b32_e32 v3, 0xc7
	v_cmp_gt_i32_e32 vcc, s2, v10
	global_load_dwordx4 v[42:45], v[4:5], off
	s_movk_i32 s2, 0x320
	v_cndmask_b32_e32 v4, v3, v10, vcc
	v_mad_u64_u32 v[4:5], s[2:3], v1, s2, v[4:5]
	v_and_b32_e32 v6, 48, v0
	v_mov_b32_e32 v7, v103
	v_ashrrev_i32_e32 v5, 31, v4
	v_lshl_add_u64 v[8:9], s[4:5], 0, v[6:7]
	v_lshlrev_b64 v[12:13], 6, v[4:5]
	v_lshl_add_u64 v[12:13], v[8:9], 0, v[12:13]
	global_load_dwordx4 v[46:49], v[12:13], off
	v_add_u32_e32 v12, 0xc8, v4
	v_ashrrev_i32_e32 v13, 31, v12
	v_lshlrev_b64 v[12:13], 6, v[12:13]
	v_lshl_add_u64 v[12:13], v[8:9], 0, v[12:13]
	global_load_dwordx4 v[50:53], v[12:13], off
	v_add_u32_e32 v12, 0x190, v4
	v_ashrrev_i32_e32 v13, 31, v12
	v_lshlrev_b64 v[12:13], 6, v[12:13]
	v_lshl_add_u64 v[12:13], v[8:9], 0, v[12:13]
	global_load_dwordx4 v[54:57], v[12:13], off
	v_add_u32_e32 v4, 0x258, v4
	v_ashrrev_i32_e32 v5, 31, v4
	v_lshlrev_b64 v[4:5], 6, v[4:5]
	v_lshl_add_u64 v[4:5], v[8:9], 0, v[4:5]
	global_load_dwordx4 v[58:61], v[4:5], off
	v_and_b32_e32 v13, 63, v0
	v_lshl_or_b32 v2, v2, 8, v13
	v_ashrrev_i32_e32 v3, 31, v2
	v_lshl_add_u64 v[2:3], v[2:3], 4, s[6:7]
	global_load_dwordx4 v[62:65], v[2:3], off
	global_load_dwordx4 v[66:69], v[2:3], off offset:1024
	global_load_dwordx4 v[70:73], v[2:3], off offset:2048
	global_load_dwordx4 v[74:77], v[2:3], off offset:3072
	s_load_dwordx4 s[4:7], s[0:1], 0x20
	v_bfe_u32 v12, v0, 6, 1
	v_lshl_add_u64 v[2:3], s[10:11], 0, v[6:7]
	v_and_b32_e32 v0, 64, v0
	v_cmp_gt_u32_e64 s[2:3], 16, v13
	s_waitcnt lgkmcnt(0)
	v_lshl_add_u64 v[4:5], s[4:5], 0, v[6:7]
	v_lshlrev_b32_e32 v6, 8, v12
	v_lshl_add_u64 v[104:105], v[2:3], 0, v[6:7]
	v_lshl_add_u64 v[106:107], v[4:5], 0, v[6:7]
	global_load_dwordx4 v[78:81], v[104:105], off
	global_load_dwordx4 v[82:85], v[104:105], off offset:64
	global_load_dwordx4 v[86:89], v[106:107], off
	global_load_dwordx4 v[90:93], v[106:107], off offset:64
	global_load_dwordx4 v[94:97], v[104:105], off offset:128
	global_load_dwordx4 v[6:9], v[104:105], off offset:192
	global_load_dwordx4 v[98:101], v[106:107], off offset:128
	global_load_dwordx4 v[2:5], v[106:107], off offset:192
	s_load_dword s6, s[6:7], 0x0
	s_waitcnt vmcnt(23)
	ds_write_b128 v102, v[14:17]
	s_waitcnt vmcnt(22)
	ds_write_b128 v102, v[18:21] offset:8192
	s_waitcnt vmcnt(21)
	ds_write_b128 v102, v[22:25] offset:16384
	s_waitcnt vmcnt(20)
	ds_write_b128 v102, v[26:29] offset:24576
	s_waitcnt vmcnt(19)
	ds_write_b128 v102, v[30:33] offset:32768
	s_waitcnt vmcnt(18)
	ds_write_b128 v102, v[34:37] offset:40960
	s_waitcnt vmcnt(17)
	ds_write_b128 v102, v[38:41] offset:49152
	s_waitcnt vmcnt(16)
	ds_write_b128 v102, v[42:45] offset:57344
	v_lshlrev_b32_e32 v14, 15, v12
	v_lshl_or_b32 v38, v13, 4, v14
	s_waitcnt lgkmcnt(0)
	s_barrier
	ds_read_b128 v[14:17], v38
	ds_read_b128 v[18:21], v38 offset:1024
	s_waitcnt vmcnt(15) lgkmcnt(1)
	v_mfma_f32_16x16x32_f16 v[14:17], v[14:17], v[46:49], 0
	ds_read_b128 v[22:25], v38 offset:2048
	ds_read_b128 v[26:29], v38 offset:10240
	ds_read_b128 v[30:33], v38 offset:18432
	s_waitcnt vmcnt(14) lgkmcnt(3)
	v_mfma_f32_16x16x32_f16 v[14:17], v[18:21], v[50:53], v[14:17]
	ds_read_b128 v[18:21], v38 offset:3072
	ds_read_b128 v[34:37], v38 offset:26624
	v_cmp_ne_u32_e64 s[4:5], 0, v0
	s_waitcnt vmcnt(13) lgkmcnt(4)
	v_mfma_f32_16x16x32_f16 v[14:17], v[22:25], v[54:57], v[14:17]
	ds_read_b128 v[22:25], v38 offset:4096
	s_and_b64 s[8:9], s[4:5], s[2:3]
	v_lshlrev_b32_e32 v0, 2, v108
	s_waitcnt vmcnt(12) lgkmcnt(2)
	v_mfma_f32_16x16x32_f16 v[14:17], v[18:21], v[58:61], v[14:17]
	ds_read_b128 v[18:21], v38 offset:5120
	s_waitcnt vmcnt(11) lgkmcnt(1)
	v_mfma_f32_16x16x32_f16 v[14:17], v[22:25], v[62:65], v[14:17]
	ds_read_b128 v[22:25], v38 offset:6144
	s_waitcnt vmcnt(10) lgkmcnt(1)
	v_mfma_f32_16x16x32_f16 v[14:17], v[18:21], v[66:69], v[14:17]
	ds_read_b128 v[18:21], v38 offset:7168
	s_waitcnt vmcnt(9) lgkmcnt(1)
	v_mfma_f32_16x16x32_f16 v[14:17], v[22:25], v[70:73], v[14:17]
	ds_read_b128 v[22:25], v38 offset:8192
	s_waitcnt vmcnt(8) lgkmcnt(1)
	v_mfma_f32_16x16x32_f16 v[14:17], v[18:21], v[74:77], v[14:17]
	ds_read_b128 v[18:21], v38 offset:9216
	s_waitcnt lgkmcnt(1)
	v_mfma_f32_16x16x32_f16 v[22:25], v[22:25], v[46:49], 0
	s_waitcnt vmcnt(7)
	s_nop 3
	v_add_f32_e32 v14, v14, v78
	v_mul_f32_e32 v14, 0x4038aa3b, v14
	v_add_f32_e32 v15, v15, v79
	s_waitcnt lgkmcnt(0)
	v_mfma_f32_16x16x32_f16 v[18:21], v[18:21], v[50:53], v[22:25]
	v_exp_f32_e32 v14, v14
	v_mul_f32_e32 v15, 0x4038aa3b, v15
	s_nop 0
	ds_read_b128 v[22:25], v38 offset:11264
	v_mfma_f32_16x16x32_f16 v[18:21], v[26:29], v[54:57], v[18:21]
	ds_read_b128 v[26:29], v38 offset:12288
	v_add_f32_e32 v16, v16, v80
	v_exp_f32_e32 v15, v15
	s_waitcnt lgkmcnt(1)
	v_mfma_f32_16x16x32_f16 v[18:21], v[22:25], v[58:61], v[18:21]
	ds_read_b128 v[22:25], v38 offset:13312
	v_mul_f32_e32 v16, 0x4038aa3b, v16
	v_add_f32_e32 v17, v17, v81
	s_waitcnt lgkmcnt(1)
	v_mfma_f32_16x16x32_f16 v[18:21], v[26:29], v[62:65], v[18:21]
	ds_read_b128 v[26:29], v38 offset:14336
	v_exp_f32_e32 v16, v16
	v_mul_f32_e32 v17, 0x4038aa3b, v17
	s_waitcnt lgkmcnt(1)
	v_mfma_f32_16x16x32_f16 v[18:21], v[22:25], v[66:69], v[18:21]
	ds_read_b128 v[22:25], v38 offset:15360
	v_exp_f32_e32 v17, v17
	v_add_f32_e32 v14, 1.0, v14
	s_waitcnt lgkmcnt(1)
	v_mfma_f32_16x16x32_f16 v[18:21], v[26:29], v[70:73], v[18:21]
	ds_read_b128 v[26:29], v38 offset:16384
	v_rcp_f32_e32 v14, v14
	v_add_f32_e32 v15, 1.0, v15
	s_waitcnt lgkmcnt(1)
	v_mfma_f32_16x16x32_f16 v[18:21], v[22:25], v[74:77], v[18:21]
	ds_read_b128 v[22:25], v38 offset:17408
	v_rcp_f32_e32 v15, v15
	v_add_f32_e32 v16, 1.0, v16
	s_waitcnt lgkmcnt(1)
	v_mfma_f32_16x16x32_f16 v[26:29], v[26:29], v[46:49], 0
	v_rcp_f32_e32 v16, v16
	v_add_f32_e32 v17, 1.0, v17
	v_rcp_f32_e32 v17, v17
	s_waitcnt lgkmcnt(0)
	v_mfma_f32_16x16x32_f16 v[22:25], v[22:25], v[50:53], v[26:29]
	v_fma_f32 v14, v14, -2.0, 1.0
	s_nop 1
	ds_read_b128 v[26:29], v38 offset:19456
	s_waitcnt vmcnt(5)
	v_fma_f32 v14, v14, v86, 0
	v_mfma_f32_16x16x32_f16 v[22:25], v[30:33], v[54:57], v[22:25]
	ds_read_b128 v[30:33], v38 offset:20480
	v_fma_f32 v15, v15, -2.0, 1.0
	v_fmac_f32_e32 v14, v15, v87
	s_waitcnt lgkmcnt(1)
	v_mfma_f32_16x16x32_f16 v[22:25], v[26:29], v[58:61], v[22:25]
	ds_read_b128 v[26:29], v38 offset:21504
	v_fma_f32 v15, v16, -2.0, 1.0
	v_fmac_f32_e32 v14, v15, v88
	s_waitcnt lgkmcnt(1)
	v_mfma_f32_16x16x32_f16 v[22:25], v[30:33], v[62:65], v[22:25]
	ds_read_b128 v[30:33], v38 offset:22528
	v_fma_f32 v15, v17, -2.0, 1.0
	v_add_f32_e32 v16, v18, v82
	s_waitcnt lgkmcnt(1)
	v_mfma_f32_16x16x32_f16 v[22:25], v[26:29], v[66:69], v[22:25]
	ds_read_b128 v[26:29], v38 offset:23552
	v_add_f32_e32 v17, v19, v83
	v_mul_f32_e32 v16, 0x4038aa3b, v16
	s_waitcnt lgkmcnt(1)
	v_mfma_f32_16x16x32_f16 v[22:25], v[30:33], v[70:73], v[22:25]
	ds_read_b128 v[30:33], v38 offset:24576
	v_mul_f32_e32 v17, 0x4038aa3b, v17
	v_exp_f32_e32 v16, v16
	s_waitcnt lgkmcnt(1)
	v_mfma_f32_16x16x32_f16 v[22:25], v[26:29], v[74:77], v[22:25]
	ds_read_b128 v[26:29], v38 offset:25600
	v_exp_f32_e32 v17, v17
	v_fmac_f32_e32 v14, v15, v89
	s_waitcnt lgkmcnt(1)
	v_mfma_f32_16x16x32_f16 v[30:33], v[30:33], v[46:49], 0
	v_add_f32_e32 v15, 1.0, v16
	v_add_f32_e32 v16, 1.0, v17
	v_add_f32_e32 v17, v20, v84
	s_waitcnt lgkmcnt(0)
	v_mfma_f32_16x16x32_f16 v[26:29], v[26:29], v[50:53], v[30:33]
	v_rcp_f32_e32 v15, v15
	s_nop 1
	ds_read_b128 v[30:33], v38 offset:27648
	v_mul_f32_e32 v17, 0x4038aa3b, v17
	v_mfma_f32_16x16x32_f16 v[26:29], v[34:37], v[54:57], v[26:29]
	ds_read_b128 v[34:37], v38 offset:28672
	v_rcp_f32_e32 v16, v16
	v_exp_f32_e32 v17, v17
	s_waitcnt lgkmcnt(1)
	v_mfma_f32_16x16x32_f16 v[26:29], v[30:33], v[58:61], v[26:29]
	ds_read_b128 v[30:33], v38 offset:29696
	v_fma_f32 v15, v15, -2.0, 1.0
	s_waitcnt vmcnt(4)
	v_fmac_f32_e32 v14, v15, v90
	v_fma_f32 v15, v16, -2.0, 1.0
	v_add_f32_e32 v16, 1.0, v17
	v_add_f32_e32 v17, v21, v85
	s_waitcnt lgkmcnt(1)
	v_mfma_f32_16x16x32_f16 v[26:29], v[34:37], v[62:65], v[26:29]
	ds_read_b128 v[34:37], v38 offset:30720
	v_rcp_f32_e32 v16, v16
	v_mul_f32_e32 v17, 0x4038aa3b, v17
	v_exp_f32_e32 v17, v17
	s_waitcnt lgkmcnt(1)
	v_mfma_f32_16x16x32_f16 v[26:29], v[30:33], v[66:69], v[26:29]
	ds_read_b128 v[30:33], v38 offset:31744
	v_fmac_f32_e32 v14, v15, v91
	v_fma_f32 v15, v16, -2.0, 1.0
	s_waitcnt vmcnt(3)
	v_add_f32_e32 v16, v22, v94
	v_fmac_f32_e32 v14, v15, v92
	v_add_f32_e32 v15, 1.0, v17
	v_mul_f32_e32 v16, 0x4038aa3b, v16
	v_add_f32_e32 v17, v23, v95
	v_exp_f32_e32 v16, v16
	v_mul_f32_e32 v17, 0x4038aa3b, v17
	v_exp_f32_e32 v17, v17
	s_waitcnt lgkmcnt(1)
	v_mfma_f32_16x16x32_f16 v[26:29], v[34:37], v[70:73], v[26:29]
	v_rcp_f32_e32 v15, v15
	v_add_f32_e32 v16, 1.0, v16
	v_rcp_f32_e32 v16, v16
	v_add_f32_e32 v17, 1.0, v17
	v_rcp_f32_e32 v17, v17
	s_waitcnt lgkmcnt(0)
	v_mfma_f32_16x16x32_f16 v[26:29], v[30:33], v[74:77], v[26:29]
	v_fma_f32 v15, v15, -2.0, 1.0
	v_fmac_f32_e32 v14, v15, v93
	v_fma_f32 v15, v16, -2.0, 1.0
	v_add_f32_e32 v16, v24, v96
	s_waitcnt vmcnt(1)
	v_fmac_f32_e32 v14, v15, v98
	v_fma_f32 v15, v17, -2.0, 1.0
	v_mul_f32_e32 v16, 0x4038aa3b, v16
	v_add_f32_e32 v17, v25, v97
	v_exp_f32_e32 v16, v16
	v_mul_f32_e32 v17, 0x4038aa3b, v17
	v_add_f32_e32 v6, v26, v6
	v_exp_f32_e32 v17, v17
	v_mul_f32_e32 v6, 0x4038aa3b, v6
	v_exp_f32_e32 v6, v6
	v_fmac_f32_e32 v14, v15, v99
	v_add_f32_e32 v15, 1.0, v16
	v_rcp_f32_e32 v15, v15
	v_add_f32_e32 v16, 1.0, v17
	v_rcp_f32_e32 v16, v16
	v_add_f32_e32 v6, 1.0, v6
	v_rcp_f32_e32 v6, v6
	v_add_f32_e32 v7, v27, v7
	v_mul_f32_e32 v7, 0x4038aa3b, v7
	v_fma_f32 v15, v15, -2.0, 1.0
	v_exp_f32_e32 v7, v7
	v_fmac_f32_e32 v14, v15, v100
	v_fma_f32 v15, v16, -2.0, 1.0
	v_fmac_f32_e32 v14, v15, v101
	v_fma_f32 v6, v6, -2.0, 1.0
	s_waitcnt vmcnt(0)
	v_fmac_f32_e32 v14, v6, v2
	v_add_f32_e32 v6, v28, v8
	v_add_f32_e32 v2, 1.0, v7
	v_mul_f32_e32 v6, 0x4038aa3b, v6
	v_add_f32_e32 v7, v29, v9
	v_exp_f32_e32 v6, v6
	v_mul_f32_e32 v7, 0x4038aa3b, v7
	v_exp_f32_e32 v7, v7
	v_rcp_f32_e32 v2, v2
	v_add_f32_e32 v6, 1.0, v6
	v_rcp_f32_e32 v6, v6
	v_add_f32_e32 v7, 1.0, v7
	v_rcp_f32_e32 v7, v7
	v_fma_f32 v2, v2, -2.0, 1.0
	v_fmac_f32_e32 v14, v2, v3
	v_fma_f32 v2, v6, -2.0, 1.0
	v_fmac_f32_e32 v14, v2, v4
	v_fma_f32 v2, v7, -2.0, 1.0
	v_fmac_f32_e32 v14, v2, v5
	v_mov_b32_e32 v2, v14
	s_nop 1
	v_permlane16_swap_b32_e32 v14, v2
	v_add_f32_e32 v2, v14, v2
	v_mov_b32_e32 v3, v2
	s_nop 1
	v_permlane32_swap_b32_e32 v2, v3
	v_add_f32_e32 v2, v2, v3
	s_and_saveexec_b64 s[4:5], s[8:9]
	v_lshl_or_b32 v3, v11, 6, v0
	v_add_u32_e32 v3, 0x10000, v3
	ds_write_b32 v3, v2
	s_or_b64 exec, exec, s[4:5]
	v_cmp_eq_u32_e64 s[4:5], 0, v12
	s_and_b64 s[2:3], s[4:5], s[2:3]
	s_and_b64 s[2:3], s[2:3], vcc
	s_waitcnt lgkmcnt(0)
	s_barrier
	s_and_saveexec_b64 s[4:5], s[2:3]
	s_cbranch_execz .LBB1_4
	v_lshl_or_b32 v0, v11, 6, v0
	v_add_u32_e32 v0, 0x10000, v0
	ds_read_b32 v0, v0
	s_load_dwordx2 s[0:1], s[0:1], 0x30
	s_movk_i32 s2, 0xc8
	s_waitcnt lgkmcnt(0)
	v_add_f32_e32 v0, v2, v0
	v_add_f32_e32 v0, s6, v0
	v_mul_f32_e32 v0, 0xbfb8aa3b, v0
	v_exp_f32_e32 v0, v0
	s_nop 0
	v_add_f32_e32 v0, 1.0, v0
	v_rcp_f32_e32 v2, v0
	v_mad_u64_u32 v[0:1], s[2:3], v1, s2, v[10:11]
	v_ashrrev_i32_e32 v1, 31, v0
	v_lshl_add_u64 v[0:1], v[0:1], 2, s[0:1]
	global_store_dword v[0:1], v2, off sc0 sc1
